# stream hand-structured v3: rows 2m,2m+1 always issued together per chunk (same DRAM pages under the assumed interleave), batched reductions, rotated wave-row
# speedup vs baseline: 1.0096x; 1.0096x over previous
.Lst_nou:
	s_or_b64 exec, exec, s[0:1]
	s_lshr_b32 s8, s3, 6
	v_and_b32_e32 v101, 63, v0
	v_lshlrev_b32_e32 v102, 4, v101
	s_add_i32 s8, s8, s2
	s_and_b32 s8, s8, 15
	s_lshl_b32 s11, s2, 7
	s_lshl_b32 s24, s2, 5
	s_add_i32 s11, s11, s8
	s_lshl_b32 s16, s11, 12
	s_add_i32 s17, s16, 0x10000
	s_add_i32 s18, s16, 0x20000
	s_add_i32 s19, s16, 0x30000
	s_add_i32 s20, s16, 0x40000
	s_add_i32 s21, s16, 0x50000
	s_add_i32 s22, s16, 0x60000
	s_add_i32 s23, s16, 0x70000
	s_waitcnt lgkmcnt(0)
	s_mov_b32 s0, s4
	s_and_b32 s1, s5, 0xffff
	s_brev_b32 s2, 16
	s_mov_b32 s3, 0x20000
	buffer_load_dwordx4 v[16:19], v102, s[0:3], s16 offen nt
	buffer_load_dwordx4 v[32:35], v102, s[0:3], s17 offen nt
	buffer_load_dwordx4 v[20:23], v102, s[0:3], s16 offen offset:1024 nt
	s_barrier
	buffer_load_dwordx4 v[36:39], v102, s[0:3], s17 offen offset:1024 nt
	buffer_load_dwordx4 v[24:27], v102, s[0:3], s16 offen offset:2048 nt
	buffer_load_dwordx4 v[40:43], v102, s[0:3], s17 offen offset:2048 nt
	buffer_load_dwordx4 v[28:31], v102, s[0:3], s16 offen offset:3072 nt
	buffer_load_dwordx4 v[44:47], v102, s[0:3], s17 offen offset:3072 nt
	ds_read_b128 v[0:3], v102
	ds_read_b128 v[4:7], v102 offset:1024
	ds_read_b128 v[8:11], v102 offset:2048
	ds_read_b128 v[12:15], v102 offset:3072
	v_mov_b32_e32 v100, 0
	s_waitcnt lgkmcnt(0)
	s_waitcnt vmcnt(7)
	v_pk_mul_f32 v[80:81], v[16:17], v[0:1]
	v_pk_mul_f32 v[82:83], v[18:19], v[2:3]
	buffer_load_dwordx4 v[48:51], v102, s[0:3], s18 offen nt
	buffer_load_dwordx4 v[64:67], v102, s[0:3], s19 offen nt
	s_waitcnt vmcnt(7)
	v_pk_fma_f32 v[80:81], v[20:21], v[4:5], v[80:81]
	v_pk_fma_f32 v[82:83], v[22:23], v[6:7], v[82:83]
	buffer_load_dwordx4 v[52:55], v102, s[0:3], s18 offen offset:1024 nt
	buffer_load_dwordx4 v[68:71], v102, s[0:3], s19 offen offset:1024 nt
	s_waitcnt vmcnt(7)
	v_pk_fma_f32 v[80:81], v[24:25], v[8:9], v[80:81]
	v_pk_fma_f32 v[82:83], v[26:27], v[10:11], v[82:83]
	buffer_load_dwordx4 v[56:59], v102, s[0:3], s18 offen offset:2048 nt
	buffer_load_dwordx4 v[72:75], v102, s[0:3], s19 offen offset:2048 nt
	s_waitcnt vmcnt(7)
	v_pk_fma_f32 v[80:81], v[28:29], v[12:13], v[80:81]
	v_pk_fma_f32 v[82:83], v[30:31], v[14:15], v[82:83]
	buffer_load_dwordx4 v[60:63], v102, s[0:3], s18 offen offset:3072 nt
	buffer_load_dwordx4 v[76:79], v102, s[0:3], s19 offen offset:3072 nt
	v_pk_add_f32 v[80:81], v[80:81], v[82:83]
	s_nop 0
	v_add_f32_e32 v84, v80, v81
	s_waitcnt vmcnt(14)
	v_pk_mul_f32 v[80:81], v[32:33], v[0:1]
	v_pk_mul_f32 v[82:83], v[34:35], v[2:3]
	s_waitcnt vmcnt(12)
	v_pk_fma_f32 v[80:81], v[36:37], v[4:5], v[80:81]
	v_pk_fma_f32 v[82:83], v[38:39], v[6:7], v[82:83]
	s_waitcnt vmcnt(10)
	v_pk_fma_f32 v[80:81], v[40:41], v[8:9], v[80:81]
	v_pk_fma_f32 v[82:83], v[42:43], v[10:11], v[82:83]
	s_waitcnt vmcnt(8)
	v_pk_fma_f32 v[80:81], v[44:45], v[12:13], v[80:81]
	v_pk_fma_f32 v[82:83], v[46:47], v[14:15], v[82:83]
	s_nop 0
	v_pk_add_f32 v[80:81], v[80:81], v[82:83]
	s_nop 0
	v_add_f32_e32 v85, v80, v81
	s_waitcnt vmcnt(7)
	v_pk_mul_f32 v[80:81], v[48:49], v[0:1]
	v_pk_mul_f32 v[82:83], v[50:51], v[2:3]
	buffer_load_dwordx4 v[16:19], v102, s[0:3], s20 offen nt
	buffer_load_dwordx4 v[32:35], v102, s[0:3], s21 offen nt
	s_waitcnt vmcnt(7)
	v_pk_fma_f32 v[80:81], v[52:53], v[4:5], v[80:81]
	v_pk_fma_f32 v[82:83], v[54:55], v[6:7], v[82:83]
	buffer_load_dwordx4 v[20:23], v102, s[0:3], s20 offen offset:1024 nt
	buffer_load_dwordx4 v[36:39], v102, s[0:3], s21 offen offset:1024 nt
	s_waitcnt vmcnt(7)
	v_pk_fma_f32 v[80:81], v[56:57], v[8:9], v[80:81]
	v_pk_fma_f32 v[82:83], v[58:59], v[10:11], v[82:83]
	buffer_load_dwordx4 v[24:27], v102, s[0:3], s20 offen offset:2048 nt
	buffer_load_dwordx4 v[40:43], v102, s[0:3], s21 offen offset:2048 nt
	s_waitcnt vmcnt(7)
	v_pk_fma_f32 v[80:81], v[60:61], v[12:13], v[80:81]
	v_pk_fma_f32 v[82:83], v[62:63], v[14:15], v[82:83]
	buffer_load_dwordx4 v[28:31], v102, s[0:3], s20 offen offset:3072 nt
	buffer_load_dwordx4 v[44:47], v102, s[0:3], s21 offen offset:3072 nt
	v_pk_add_f32 v[80:81], v[80:81], v[82:83]
	s_nop 0
	v_add_f32_e32 v86, v80, v81
	s_waitcnt vmcnt(14)
	v_pk_mul_f32 v[80:81], v[64:65], v[0:1]
	v_pk_mul_f32 v[82:83], v[66:67], v[2:3]
	s_waitcnt vmcnt(12)
	v_pk_fma_f32 v[80:81], v[68:69], v[4:5], v[80:81]
	v_pk_fma_f32 v[82:83], v[70:71], v[6:7], v[82:83]
	s_waitcnt vmcnt(10)
	v_pk_fma_f32 v[80:81], v[72:73], v[8:9], v[80:81]
	v_pk_fma_f32 v[82:83], v[74:75], v[10:11], v[82:83]
	s_waitcnt vmcnt(8)
	v_pk_fma_f32 v[80:81], v[76:77], v[12:13], v[80:81]
	v_pk_fma_f32 v[82:83], v[78:79], v[14:15], v[82:83]
	s_nop 0
	v_pk_add_f32 v[80:81], v[80:81], v[82:83]
	s_nop 0
	v_add_f32_e32 v87, v80, v81
	s_nop 0
	v_add_f32_dpp v84, v84, v84 quad_perm:[1,0,3,2] row_mask:0xf bank_mask:0xf bound_ctrl:1
	v_add_f32_dpp v85, v85, v85 quad_perm:[1,0,3,2] row_mask:0xf bank_mask:0xf bound_ctrl:1
	v_add_f32_dpp v86, v86, v86 quad_perm:[1,0,3,2] row_mask:0xf bank_mask:0xf bound_ctrl:1
	v_add_f32_dpp v87, v87, v87 quad_perm:[1,0,3,2] row_mask:0xf bank_mask:0xf bound_ctrl:1
	v_add_f32_dpp v84, v84, v84 quad_perm:[2,3,0,1] row_mask:0xf bank_mask:0xf bound_ctrl:1
	v_add_f32_dpp v85, v85, v85 quad_perm:[2,3,0,1] row_mask:0xf bank_mask:0xf bound_ctrl:1
	v_add_f32_dpp v86, v86, v86 quad_perm:[2,3,0,1] row_mask:0xf bank_mask:0xf bound_ctrl:1
	v_add_f32_dpp v87, v87, v87 quad_perm:[2,3,0,1] row_mask:0xf bank_mask:0xf bound_ctrl:1
	v_add_f32_dpp v84, v84, v84 row_ror:4 row_mask:0xf bank_mask:0xf bound_ctrl:1
	v_add_f32_dpp v85, v85, v85 row_ror:4 row_mask:0xf bank_mask:0xf bound_ctrl:1
	v_add_f32_dpp v86, v86, v86 row_ror:4 row_mask:0xf bank_mask:0xf bound_ctrl:1
	v_add_f32_dpp v87, v87, v87 row_ror:4 row_mask:0xf bank_mask:0xf bound_ctrl:1
	v_add_f32_dpp v84, v84, v84 row_ror:8 row_mask:0xf bank_mask:0xf bound_ctrl:1
	v_add_f32_dpp v85, v85, v85 row_ror:8 row_mask:0xf bank_mask:0xf bound_ctrl:1
	v_add_f32_dpp v86, v86, v86 row_ror:8 row_mask:0xf bank_mask:0xf bound_ctrl:1
	v_add_f32_dpp v87, v87, v87 row_ror:8 row_mask:0xf bank_mask:0xf bound_ctrl:1
	v_mov_b32_e32 v92, v84
	v_mov_b32_e32 v93, v85
	v_mov_b32_e32 v94, v86
	v_mov_b32_e32 v95, v87
	v_permlane16_swap_b32_e32 v84, v92
	v_permlane16_swap_b32_e32 v85, v93
	v_permlane16_swap_b32_e32 v86, v94
	v_permlane16_swap_b32_e32 v87, v95
	v_add_f32_e32 v84, v84, v92
	v_add_f32_e32 v85, v85, v93
	v_add_f32_e32 v86, v86, v94
	v_add_f32_e32 v87, v87, v95
	v_mov_b32_e32 v92, v84
	v_mov_b32_e32 v93, v85
	v_mov_b32_e32 v94, v86
	v_mov_b32_e32 v95, v87
	v_permlane32_swap_b32_e32 v84, v92
	v_permlane32_swap_b32_e32 v85, v93
	v_permlane32_swap_b32_e32 v86, v94
	v_permlane32_swap_b32_e32 v87, v95
	v_add_f32_e32 v84, v84, v92
	v_add_f32_e32 v85, v85, v93
	v_add_f32_e32 v86, v86, v94
	v_add_f32_e32 v87, v87, v95
	v_cmp_eq_u32_e32 vcc, 0, v101
	s_nop 1
	v_cndmask_b32_e32 v100, v100, v84, vcc
	v_cmp_eq_u32_e32 vcc, 1, v101
	s_nop 1
	v_cndmask_b32_e32 v100, v100, v85, vcc
	v_cmp_eq_u32_e32 vcc, 2, v101
	s_nop 1
	v_cndmask_b32_e32 v100, v100, v86, vcc
	v_cmp_eq_u32_e32 vcc, 3, v101
	s_nop 1
	v_cndmask_b32_e32 v100, v100, v87, vcc
	s_waitcnt vmcnt(7)
	v_pk_mul_f32 v[80:81], v[16:17], v[0:1]
	v_pk_mul_f32 v[82:83], v[18:19], v[2:3]
	buffer_load_dwordx4 v[48:51], v102, s[0:3], s22 offen nt
	buffer_load_dwordx4 v[64:67], v102, s[0:3], s23 offen nt
	s_waitcnt vmcnt(7)
	v_pk_fma_f32 v[80:81], v[20:21], v[4:5], v[80:81]
	v_pk_fma_f32 v[82:83], v[22:23], v[6:7], v[82:83]
	buffer_load_dwordx4 v[52:55], v102, s[0:3], s22 offen offset:1024 nt
	buffer_load_dwordx4 v[68:71], v102, s[0:3], s23 offen offset:1024 nt
	s_waitcnt vmcnt(7)
	v_pk_fma_f32 v[80:81], v[24:25], v[8:9], v[80:81]
	v_pk_fma_f32 v[82:83], v[26:27], v[10:11], v[82:83]
	buffer_load_dwordx4 v[56:59], v102, s[0:3], s22 offen offset:2048 nt
	buffer_load_dwordx4 v[72:75], v102, s[0:3], s23 offen offset:2048 nt
	s_waitcnt vmcnt(7)
	v_pk_fma_f32 v[80:81], v[28:29], v[12:13], v[80:81]
	v_pk_fma_f32 v[82:83], v[30:31], v[14:15], v[82:83]
	buffer_load_dwordx4 v[60:63], v102, s[0:3], s22 offen offset:3072 nt
	buffer_load_dwordx4 v[76:79], v102, s[0:3], s23 offen offset:3072 nt
	v_pk_add_f32 v[80:81], v[80:81], v[82:83]
	s_nop 0
	v_add_f32_e32 v88, v80, v81
	s_waitcnt vmcnt(14)
	v_pk_mul_f32 v[80:81], v[32:33], v[0:1]
	v_pk_mul_f32 v[82:83], v[34:35], v[2:3]
	s_waitcnt vmcnt(12)
	v_pk_fma_f32 v[80:81], v[36:37], v[4:5], v[80:81]
	v_pk_fma_f32 v[82:83], v[38:39], v[6:7], v[82:83]
	s_waitcnt vmcnt(10)
	v_pk_fma_f32 v[80:81], v[40:41], v[8:9], v[80:81]
	v_pk_fma_f32 v[82:83], v[42:43], v[10:11], v[82:83]
	s_waitcnt vmcnt(8)
	v_pk_fma_f32 v[80:81], v[44:45], v[12:13], v[80:81]
	v_pk_fma_f32 v[82:83], v[46:47], v[14:15], v[82:83]
	s_nop 0
	v_pk_add_f32 v[80:81], v[80:81], v[82:83]
	s_nop 0
	v_add_f32_e32 v89, v80, v81
	s_waitcnt vmcnt(7)
	v_pk_mul_f32 v[80:81], v[48:49], v[0:1]
	v_pk_mul_f32 v[82:83], v[50:51], v[2:3]
	s_waitcnt vmcnt(5)
	v_pk_fma_f32 v[80:81], v[52:53], v[4:5], v[80:81]
	v_pk_fma_f32 v[82:83], v[54:55], v[6:7], v[82:83]
	s_waitcnt vmcnt(3)
	v_pk_fma_f32 v[80:81], v[56:57], v[8:9], v[80:81]
	v_pk_fma_f32 v[82:83], v[58:59], v[10:11], v[82:83]
	s_waitcnt vmcnt(1)
	v_pk_fma_f32 v[80:81], v[60:61], v[12:13], v[80:81]
	v_pk_fma_f32 v[82:83], v[62:63], v[14:15], v[82:83]
	s_nop 0
	v_pk_add_f32 v[80:81], v[80:81], v[82:83]
	s_nop 0
	v_add_f32_e32 v90, v80, v81
	s_waitcnt vmcnt(6)
	v_pk_mul_f32 v[80:81], v[64:65], v[0:1]
	v_pk_mul_f32 v[82:83], v[66:67], v[2:3]
	s_waitcnt vmcnt(4)
	v_pk_fma_f32 v[80:81], v[68:69], v[4:5], v[80:81]
	v_pk_fma_f32 v[82:83], v[70:71], v[6:7], v[82:83]
	s_waitcnt vmcnt(2)
	v_pk_fma_f32 v[80:81], v[72:73], v[8:9], v[80:81]
	v_pk_fma_f32 v[82:83], v[74:75], v[10:11], v[82:83]
	s_waitcnt vmcnt(0)
	v_pk_fma_f32 v[80:81], v[76:77], v[12:13], v[80:81]
	v_pk_fma_f32 v[82:83], v[78:79], v[14:15], v[82:83]
	s_nop 0
	v_pk_add_f32 v[80:81], v[80:81], v[82:83]
	s_nop 0
	v_add_f32_e32 v91, v80, v81
	s_nop 0
	v_add_f32_dpp v88, v88, v88 quad_perm:[1,0,3,2] row_mask:0xf bank_mask:0xf bound_ctrl:1
	v_add_f32_dpp v89, v89, v89 quad_perm:[1,0,3,2] row_mask:0xf bank_mask:0xf bound_ctrl:1
	v_add_f32_dpp v90, v90, v90 quad_perm:[1,0,3,2] row_mask:0xf bank_mask:0xf bound_ctrl:1
	v_add_f32_dpp v91, v91, v91 quad_perm:[1,0,3,2] row_mask:0xf bank_mask:0xf bound_ctrl:1
	v_add_f32_dpp v88, v88, v88 quad_perm:[2,3,0,1] row_mask:0xf bank_mask:0xf bound_ctrl:1
	v_add_f32_dpp v89, v89, v89 quad_perm:[2,3,0,1] row_mask:0xf bank_mask:0xf bound_ctrl:1
	v_add_f32_dpp v90, v90, v90 quad_perm:[2,3,0,1] row_mask:0xf bank_mask:0xf bound_ctrl:1
	v_add_f32_dpp v91, v91, v91 quad_perm:[2,3,0,1] row_mask:0xf bank_mask:0xf bound_ctrl:1
	v_add_f32_dpp v88, v88, v88 row_ror:4 row_mask:0xf bank_mask:0xf bound_ctrl:1
	v_add_f32_dpp v89, v89, v89 row_ror:4 row_mask:0xf bank_mask:0xf bound_ctrl:1
	v_add_f32_dpp v90, v90, v90 row_ror:4 row_mask:0xf bank_mask:0xf bound_ctrl:1
	v_add_f32_dpp v91, v91, v91 row_ror:4 row_mask:0xf bank_mask:0xf bound_ctrl:1
	v_add_f32_dpp v88, v88, v88 row_ror:8 row_mask:0xf bank_mask:0xf bound_ctrl:1
	v_add_f32_dpp v89, v89, v89 row_ror:8 row_mask:0xf bank_mask:0xf bound_ctrl:1
	v_add_f32_dpp v90, v90, v90 row_ror:8 row_mask:0xf bank_mask:0xf bound_ctrl:1
	v_add_f32_dpp v91, v91, v91 row_ror:8 row_mask:0xf bank_mask:0xf bound_ctrl:1
	v_mov_b32_e32 v92, v88
	v_mov_b32_e32 v93, v89
	v_mov_b32_e32 v94, v90
	v_mov_b32_e32 v95, v91
	v_permlane16_swap_b32_e32 v88, v92
	v_permlane16_swap_b32_e32 v89, v93
	v_permlane16_swap_b32_e32 v90, v94
	v_permlane16_swap_b32_e32 v91, v95
	v_add_f32_e32 v88, v88, v92
	v_add_f32_e32 v89, v89, v93
	v_add_f32_e32 v90, v90, v94
	v_add_f32_e32 v91, v91, v95
	v_mov_b32_e32 v92, v88
	v_mov_b32_e32 v93, v89
	v_mov_b32_e32 v94, v90
	v_mov_b32_e32 v95, v91
	v_permlane32_swap_b32_e32 v88, v92
	v_permlane32_swap_b32_e32 v89, v93
	v_permlane32_swap_b32_e32 v90, v94
	v_permlane32_swap_b32_e32 v91, v95
	v_add_f32_e32 v88, v88, v92
	v_add_f32_e32 v89, v89, v93
	v_add_f32_e32 v90, v90, v94
	v_add_f32_e32 v91, v91, v95
	v_cmp_eq_u32_e32 vcc, 4, v101
	s_nop 1
	v_cndmask_b32_e32 v100, v100, v88, vcc
	v_cmp_eq_u32_e32 vcc, 5, v101
	s_nop 1
	v_cndmask_b32_e32 v100, v100, v89, vcc
	v_cmp_eq_u32_e32 vcc, 6, v101
	s_nop 1
	v_cndmask_b32_e32 v100, v100, v90, vcc
	v_cmp_eq_u32_e32 vcc, 7, v101
	s_nop 1
	v_cndmask_b32_e32 v100, v100, v91, vcc
	v_cmp_gt_u32_e32 vcc, 8, v101
	s_and_saveexec_b64 s[0:1], vcc
	v_lshlrev_b32_e32 v92, 2, v101
	s_lshl_b32 s9, s8, 13
	s_add_i32 s9, s9, s24
	s_addk_i32 s9, 0x6040
	v_add_u32_e32 v92, s9, v92
	global_store_dword v92, v100, s[6:7]
	s_endpgm

	.amdhsa_kernel _Z13stream_kernelPKfPf
		.amdhsa_group_segment_fixed_size 4096
		.amdhsa_private_segment_fixed_size 0
		.amdhsa_kernarg_size 16
		.amdhsa_user_sgpr_count 2
		.amdhsa_user_sgpr_dispatch_ptr 0
		.amdhsa_user_sgpr_queue_ptr 0
		.amdhsa_user_sgpr_kernarg_segment_ptr 1
		.amdhsa_user_sgpr_dispatch_id 0
		.amdhsa_user_sgpr_kernarg_preload_length 0
		.amdhsa_user_sgpr_kernarg_preload_offset 0
		.amdhsa_user_sgpr_private_segment_size 0
		.amdhsa_uses_dynamic_stack 0
		.amdhsa_enable_private_segment 0
		.amdhsa_system_sgpr_workgroup_id_x 1
		.amdhsa_system_sgpr_workgroup_id_y 0
		.amdhsa_system_sgpr_workgroup_id_z 0
		.amdhsa_system_sgpr_workgroup_info 0
		.amdhsa_system_vgpr_workitem_id 0
		.amdhsa_next_free_vgpr 103
		.amdhsa_next_free_sgpr 25
		.amdhsa_accum_offset 104
		.amdhsa_reserve_vcc 1
		.amdhsa_float_round_mode_32 0
		.amdhsa_float_round_mode_16_64 0
		.amdhsa_float_denorm_mode_32 3
		.amdhsa_float_denorm_mode_16_64 3
		.amdhsa_dx10_clamp 1
		.amdhsa_ieee_mode 1
		.amdhsa_fp16_overflow 0
		.amdhsa_tg_split 0
		.amdhsa_exception_fp_ieee_invalid_op 0
		.amdhsa_exception_fp_denorm_src 0
		.amdhsa_exception_fp_ieee_div_zero 0
		.amdhsa_exception_fp_ieee_overflow 0
		.amdhsa_exception_fp_ieee_underflow 0
		.amdhsa_exception_fp_ieee_inexact 0
		.amdhsa_exception_int_div_zero 0
	.end_amdhsa_kernel

.Lfunc_end1:
	.size	_Z13stream_kernelPKfPf, .Lfunc_end1-_Z13stream_kernelPKfPf
	.set _Z13stream_kernelPKfPf.num_vgpr, 103
	.set _Z13stream_kernelPKfPf.num_agpr, 0
	.set _Z13stream_kernelPKfPf.numbered_sgpr, 25
	.set _Z13stream_kernelPKfPf.num_named_barrier, 0
	.set _Z13stream_kernelPKfPf.private_seg_size, 0
	.set _Z13stream_kernelPKfPf.uses_vcc, 1
	.set _Z13stream_kernelPKfPf.uses_flat_scratch, 0
	.set _Z13stream_kernelPKfPf.has_dyn_sized_stack, 0
	.set _Z13stream_kernelPKfPf.has_recursion, 0
	.set _Z13stream_kernelPKfPf.has_indirect_call, 0

amdhsa.kernels:
  - .agpr_count:     0
    .args:
      - .actual_access:  read_only
        .address_space:  global
        .offset:         0
        .size:           8
        .value_kind:     global_buffer
      - .actual_access:  read_only
        .address_space:  global
        .offset:         8
        .size:           8
        .value_kind:     global_buffer
      - .actual_access:  read_only
        .address_space:  global
        .offset:         16
        .size:           8
        .value_kind:     global_buffer
      - .actual_access:  read_only
        .address_space:  global
        .offset:         24
        .size:           8
        .value_kind:     global_buffer
      - .actual_access:  write_only
        .address_space:  global
        .offset:         32
        .size:           8
        .value_kind:     global_buffer
    .group_segment_fixed_size: 2112
    .kernarg_segment_align: 8
    .kernarg_segment_size: 40
    .language:       OpenCL C
    .language_version:
      - 2
      - 0
    .max_flat_workgroup_size: 1024
    .name:           _Z11prep_kernelPKfS0_S0_S0_Pf
    .private_segment_fixed_size: 0
    .sgpr_count:     32
    .sgpr_spill_count: 0
    .symbol:         _Z11prep_kernelPKfS0_S0_S0_Pf.kd
    .uniform_work_group_size: 1
    .uses_dynamic_stack: false
    .vgpr_count:     40
    .vgpr_spill_count: 0
    .wavefront_size: 64
  - .agpr_count:     0
    .args:
      - .actual_access:  read_only
        .address_space:  global
        .offset:         0
        .size:           8
        .value_kind:     global_buffer
      - .address_space:  global
        .offset:         8
        .size:           8
        .value_kind:     global_buffer
    .group_segment_fixed_size: 4096
    .kernarg_segment_align: 8
    .kernarg_segment_size: 16
    .language:       OpenCL C
    .language_version:
      - 2
      - 0
    .max_flat_workgroup_size: 1024
    .name:           _Z13stream_kernelPKfPf
    .private_segment_fixed_size: 0
    .sgpr_count:     31
    .sgpr_spill_count: 0
    .symbol:         _Z13stream_kernelPKfPf.kd
    .uniform_work_group_size: 1
    .uses_dynamic_stack: false
    .vgpr_count:     103
    .vgpr_spill_count: 0
    .wavefront_size: 64
  - .agpr_count:     0
    .args:
      - .actual_access:  read_only
        .address_space:  global
        .offset:         0
        .size:           8
        .value_kind:     global_buffer
      - .actual_access:  write_only
        .address_space:  global
        .offset:         8
        .size:           8
        .value_kind:     global_buffer
    .group_segment_fixed_size: 32
    .kernarg_segment_align: 8
    .kernarg_segment_size: 16
    .language:       OpenCL C
    .language_version:
      - 2
      - 0
    .max_flat_workgroup_size: 256
    .name:           _Z14softmax_kernelPKfPf
    .private_segment_fixed_size: 0
    .sgpr_count:     16
    .sgpr_spill_count: 0
    .symbol:         _Z14softmax_kernelPKfPf.kd
    .uniform_work_group_size: 1
    .uses_dynamic_stack: false
    .vgpr_count:     17
    .vgpr_spill_count: 0
    .wavefront_size: 64
